# baseline (speedup 1.0000x reference)
.Lpl0_done:
.LBB1_87:
	s_cmp_lt_u32 s25, 12
	s_cbranch_scc0 .Lp0_pay
	buffer_load_dwordx4 v[54:57], v194, s[20:23], 0 offen sc1
	buffer_load_dwordx4 v[50:53], v195, s[20:23], 0 offen sc1
	buffer_load_dwordx4 v[46:49], v196, s[20:23], 0 offen sc1
	buffer_load_dwordx4 v[42:45], v197, s[20:23], 0 offen sc1
	buffer_load_dwordx4 v[38:41], v198, s[20:23], 0 offen sc1
	buffer_load_dwordx4 v[34:37], v199, s[20:23], 0 offen sc1
	s_waitcnt vmcnt(10) lgkmcnt(0)
	s_and_saveexec_b64 s[68:69], s[6:7]
	v_add_u32_e32 v0, 0x8400, v60
	ds_write2_b32 v0, v181, v184 offset1:16
	ds_write_b32 v60, v185 offset:33920
	s_mov_b64 exec, s[68:69]
	s_waitcnt lgkmcnt(0)
	s_barrier
	s_branch .LBB1_106
